# baseline (speedup 1.0000x reference)
.LBB2_169:
	ds_read_u16 v0, v102
	s_waitcnt lgkmcnt(0)
	v_and_b32_e32 v105, 0xffff, v0
	v_lshrrev_b32_e32 v250, 11, v105
	v_bfe_u32 v251, v105, 8, 3
	v_mad_u32_u24 v250, v250, 10, v251
	v_lshlrev_b32_e32 v250, 9, v250
	v_lshl_add_u32 v250, v97, 4, v250
	v_add_u32_e32 v250, 0x13e00, v250
	v_mul_lo_u16_sdwa v0, v0, s6 dst_sel:DWORD dst_unused:UNUSED_PAD src0_sel:BYTE_0 src1_sel:DWORD
	v_lshrrev_b32_e32 v50, 11, v105
	v_bfe_u32 v54, v105, 8, 3
	v_lshrrev_b16_e32 v52, 10, v0
	v_and_b32_e32 v104, 0xff, v105
	v_add_u32_e32 v55, s12, v54
	v_mul_i32_i24_e32 v0, -13, v52
	v_add_u32_e32 v56, s11, v50
	v_add3_u32 v57, v104, v96, v0
	v_med3_i32 v0, v56, 0, 63
	v_med3_i32 v50, v55, 0, 63
	v_add_lshl_u32 v60, s10, v52, 6
	v_lshlrev_b32_e32 v58, 15, v0
	v_lshlrev_b32_e32 v59, 9, v50
	v_add_u32_e32 v52, v57, v60
	v_or_b32_e32 v0, v58, v59
	v_ashrrev_i32_e32 v53, 31, v52
	v_lshl_add_u64 v[50:51], v[88:89], 0, v[0:1]
	v_lshlrev_b64 v[52:53], 9, v[52:53]
	v_lshl_add_u64 v[52:53], v[90:91], 0, v[52:53]
	ds_read_b128 v[106:109], v250 offset:256
	ds_read_b128 v[70:73], v250
	global_load_dwordx4 v[116:119], v[52:53], off offset:16
	global_load_dwordx4 v[120:123], v[52:53], off
	v_or_b32_e32 v0, s33, v54
	v_add_u32_e32 v61, 1, v57
	v_lshlrev_b32_e32 v54, 9, v0
	v_add_u32_e32 v52, v61, v60
	v_or_b32_e32 v0, v58, v54
	v_ashrrev_i32_e32 v53, 31, v52
	v_lshl_add_u64 v[50:51], v[88:89], 0, v[0:1]
	v_lshlrev_b64 v[52:53], 9, v[52:53]
	v_lshl_add_u64 v[52:53], v[90:91], 0, v[52:53]
	ds_read_b128 v[124:127], v250 offset:768
	ds_read_b128 v[128:131], v250 offset:512
	global_load_dwordx4 v[132:135], v[52:53], off offset:16
	global_load_dwordx4 v[136:139], v[52:53], off
	v_max_i32_e32 v0, -2, v55
	v_add_u32_e32 v0, 2, v0
	v_min_u32_e32 v0, 63, v0
	v_add_u32_e32 v64, 2, v57
	v_lshlrev_b32_e32 v62, 9, v0
	v_add_u32_e32 v52, v64, v60
	v_or_b32_e32 v0, v58, v62
	v_ashrrev_i32_e32 v53, 31, v52
	v_lshl_add_u64 v[50:51], v[88:89], 0, v[0:1]
	v_lshlrev_b64 v[52:53], 9, v[52:53]
	v_lshl_add_u64 v[52:53], v[90:91], 0, v[52:53]
	ds_read_b128 v[140:143], v250 offset:1280
	ds_read_b128 v[144:147], v250 offset:1024
	global_load_dwordx4 v[148:151], v[52:53], off offset:16
	global_load_dwordx4 v[152:155], v[52:53], off
	v_max_i32_e32 v0, -1, v56
	v_add_u32_e32 v0, 1, v0
	v_min_u32_e32 v0, 63, v0
	v_add_u32_e32 v58, 64, v60
	v_lshlrev_b32_e32 v55, 15, v0
	v_add_u32_e32 v52, v57, v58
	v_or_b32_e32 v0, v55, v59
	v_ashrrev_i32_e32 v53, 31, v52
	v_lshl_add_u64 v[50:51], v[88:89], 0, v[0:1]
	v_lshlrev_b64 v[52:53], 9, v[52:53]
	v_lshl_add_u64 v[52:53], v[90:91], 0, v[52:53]
	ds_read_b128 v[156:159], v250 offset:5376
	ds_read_b128 v[160:163], v250 offset:5120
	global_load_dwordx4 v[164:167], v[52:53], off offset:16
	global_load_dwordx4 v[168:171], v[52:53], off
	v_add_u32_e32 v52, v61, v58
	v_or_b32_e32 v0, v55, v54
	v_ashrrev_i32_e32 v53, 31, v52
	v_lshl_add_u64 v[50:51], v[88:89], 0, v[0:1]
	v_lshlrev_b64 v[52:53], 9, v[52:53]
	v_lshl_add_u64 v[52:53], v[90:91], 0, v[52:53]
	ds_read_b128 v[172:175], v250 offset:5888
	ds_read_b128 v[176:179], v250 offset:5632
	global_load_dwordx4 v[180:183], v[52:53], off offset:16
	global_load_dwordx4 v[184:187], v[52:53], off
	v_add_u32_e32 v52, v64, v58
	v_or_b32_e32 v0, v55, v62
	v_ashrrev_i32_e32 v53, 31, v52
	v_lshl_add_u64 v[50:51], v[88:89], 0, v[0:1]
	v_lshlrev_b64 v[52:53], 9, v[52:53]
	v_lshl_add_u64 v[52:53], v[90:91], 0, v[52:53]
	ds_read_b128 v[188:191], v250 offset:6400
	ds_read_b128 v[192:195], v250 offset:6144
	global_load_dwordx4 v[196:199], v[52:53], off offset:16
	global_load_dwordx4 v[200:203], v[52:53], off
	v_max_i32_e32 v0, -2, v56
	v_add_u32_e32 v0, 2, v0
	v_min_u32_e32 v0, 63, v0
	v_add_u32_e32 v65, 0x80, v60
	v_lshlrev_b32_e32 v63, 15, v0
	v_add_u32_e32 v52, v57, v65
	v_or_b32_e32 v0, v63, v59
	v_ashrrev_i32_e32 v53, 31, v52
	v_lshl_add_u64 v[50:51], v[88:89], 0, v[0:1]
	v_lshlrev_b64 v[52:53], 9, v[52:53]
	v_lshl_add_u64 v[52:53], v[90:91], 0, v[52:53]
	ds_read_b128 v[74:77], v250 offset:10496
	ds_read_b128 v[204:207], v250 offset:10240
	global_load_dwordx4 v[82:85], v[52:53], off offset:16
	global_load_dwordx4 v[208:211], v[52:53], off
	v_add_u32_e32 v52, v61, v65
	v_or_b32_e32 v0, v63, v54
	v_ashrrev_i32_e32 v53, 31, v52
	v_lshl_add_u64 v[50:51], v[88:89], 0, v[0:1]
	v_lshlrev_b64 v[52:53], 9, v[52:53]
	v_lshl_add_u64 v[52:53], v[90:91], 0, v[52:53]
	s_waitcnt lgkmcnt(13)
	ds_read_b128 v[54:57], v250 offset:11008
	ds_read_b128 v[66:69], v250 offset:10752
	global_load_dwordx4 v[58:61], v[52:53], off offset:16
	global_load_dwordx4 v[78:81], v[52:53], off
	v_add_u32_e32 v50, v64, v65
	v_ashrrev_i32_e32 v51, 31, v50
	v_lshlrev_b64 v[50:51], 9, v[50:51]
	v_lshl_add_u64 v[110:111], v[90:91], 0, v[50:51]
	v_or_b32_e32 v0, v63, v62
	v_lshl_add_u64 v[62:63], v[88:89], 0, v[0:1]
	s_waitcnt lgkmcnt(13)
	v_cvt_f64_f32_e32 v[50:51], v70
	s_waitcnt vmcnt(14)
	v_cvt_f64_f32_e32 v[52:53], v120
	v_fma_f64 v[92:93], v[50:51], v[52:53], 0
	v_cvt_f64_f32_e32 v[50:51], v72
	v_cvt_f64_f32_e32 v[52:53], v122
	v_fmac_f64_e32 v[92:93], v[50:51], v[52:53]
	v_cvt_f64_f32_e32 v[50:51], v71
	v_cvt_f64_f32_e32 v[52:53], v121
	v_fma_f64 v[94:95], v[50:51], v[52:53], 0
	v_cvt_f64_f32_e32 v[70:71], v73
	v_cvt_f64_f32_e32 v[72:73], v123
	v_fmac_f64_e32 v[94:95], v[70:71], v[72:73]
	v_cvt_f64_f32_e32 v[70:71], v106
	v_cvt_f64_f32_e32 v[72:73], v116
	v_fmac_f64_e32 v[92:93], v[70:71], v[72:73]
	v_cvt_f64_f32_e32 v[70:71], v107
	v_cvt_f64_f32_e32 v[72:73], v117
	v_fmac_f64_e32 v[94:95], v[70:71], v[72:73]
	v_cvt_f64_f32_e32 v[70:71], v108
	v_cvt_f64_f32_e32 v[72:73], v118
	s_waitcnt lgkmcnt(13)
	ds_read_b128 v[50:53], v250 offset:11520
	s_nop 0
	ds_read_b128 v[62:65], v250 offset:11264
	v_fmac_f64_e32 v[92:93], v[70:71], v[72:73]
	global_load_dwordx4 v[70:73], v[110:111], off offset:16
	global_load_dwordx4 v[120:123], v[110:111], off
	v_cvt_f64_f32_e32 v[106:107], v109
	v_cvt_f64_f32_e32 v[108:109], v119
	v_fmac_f64_e32 v[94:95], v[106:107], v[108:109]
	s_waitcnt lgkmcnt(13)
	v_cvt_f64_f32_e32 v[106:107], v128
	s_waitcnt vmcnt(14)
	v_cvt_f64_f32_e32 v[108:109], v136
	v_fmac_f64_e32 v[92:93], v[106:107], v[108:109]
	v_cvt_f64_f32_e32 v[106:107], v129
	v_cvt_f64_f32_e32 v[108:109], v137
	v_fmac_f64_e32 v[94:95], v[106:107], v[108:109]
	v_cvt_f64_f32_e32 v[106:107], v130
	v_cvt_f64_f32_e32 v[108:109], v138
	v_fmac_f64_e32 v[92:93], v[106:107], v[108:109]
	v_cvt_f64_f32_e32 v[106:107], v131
	v_cvt_f64_f32_e32 v[108:109], v139
	v_fmac_f64_e32 v[94:95], v[106:107], v[108:109]
	v_cvt_f64_f32_e32 v[106:107], v124
	v_cvt_f64_f32_e32 v[108:109], v132
	v_fmac_f64_e32 v[92:93], v[106:107], v[108:109]
	v_cvt_f64_f32_e32 v[106:107], v125
	v_cvt_f64_f32_e32 v[108:109], v133
	v_fmac_f64_e32 v[94:95], v[106:107], v[108:109]
	v_cvt_f64_f32_e32 v[106:107], v126
	v_cvt_f64_f32_e32 v[108:109], v134
	v_fmac_f64_e32 v[92:93], v[106:107], v[108:109]
	v_cvt_f64_f32_e32 v[106:107], v127
	v_cvt_f64_f32_e32 v[108:109], v135
	v_fmac_f64_e32 v[94:95], v[106:107], v[108:109]
	s_waitcnt lgkmcnt(12)
	v_cvt_f64_f32_e32 v[106:107], v144
	s_waitcnt vmcnt(12)
	v_cvt_f64_f32_e32 v[108:109], v152
	v_fmac_f64_e32 v[92:93], v[106:107], v[108:109]
	v_cvt_f64_f32_e32 v[106:107], v145
	v_cvt_f64_f32_e32 v[108:109], v153
	v_fmac_f64_e32 v[94:95], v[106:107], v[108:109]
	v_cvt_f64_f32_e32 v[106:107], v146
	v_cvt_f64_f32_e32 v[108:109], v154
	v_fmac_f64_e32 v[92:93], v[106:107], v[108:109]
	v_cvt_f64_f32_e32 v[106:107], v147
	v_cvt_f64_f32_e32 v[108:109], v155
	v_fmac_f64_e32 v[94:95], v[106:107], v[108:109]
	v_cvt_f64_f32_e32 v[106:107], v140
	v_cvt_f64_f32_e32 v[108:109], v148
	v_fmac_f64_e32 v[92:93], v[106:107], v[108:109]
	v_cvt_f64_f32_e32 v[106:107], v141
	v_cvt_f64_f32_e32 v[108:109], v149
	v_fmac_f64_e32 v[94:95], v[106:107], v[108:109]
	v_cvt_f64_f32_e32 v[106:107], v142
	v_cvt_f64_f32_e32 v[108:109], v150
	v_fmac_f64_e32 v[92:93], v[106:107], v[108:109]
	v_cvt_f64_f32_e32 v[106:107], v143
	v_cvt_f64_f32_e32 v[108:109], v151
	v_fmac_f64_e32 v[94:95], v[106:107], v[108:109]
	s_waitcnt lgkmcnt(10)
	v_cvt_f64_f32_e32 v[106:107], v160
	s_waitcnt vmcnt(10)
	v_cvt_f64_f32_e32 v[108:109], v168
	v_fmac_f64_e32 v[92:93], v[106:107], v[108:109]
	v_cvt_f64_f32_e32 v[106:107], v161
	v_cvt_f64_f32_e32 v[108:109], v169
	v_fmac_f64_e32 v[94:95], v[106:107], v[108:109]
	v_cvt_f64_f32_e32 v[106:107], v162
	v_cvt_f64_f32_e32 v[108:109], v170
	v_fmac_f64_e32 v[92:93], v[106:107], v[108:109]
	v_cvt_f64_f32_e32 v[106:107], v163
	v_cvt_f64_f32_e32 v[108:109], v171
	v_fmac_f64_e32 v[94:95], v[106:107], v[108:109]
	v_cvt_f64_f32_e32 v[106:107], v156
	v_cvt_f64_f32_e32 v[108:109], v164
	v_fmac_f64_e32 v[92:93], v[106:107], v[108:109]
	v_cvt_f64_f32_e32 v[106:107], v157
	v_cvt_f64_f32_e32 v[108:109], v165
	v_fmac_f64_e32 v[94:95], v[106:107], v[108:109]
	v_cvt_f64_f32_e32 v[106:107], v158
	v_cvt_f64_f32_e32 v[108:109], v166
	v_fmac_f64_e32 v[92:93], v[106:107], v[108:109]
	v_cvt_f64_f32_e32 v[106:107], v159
	v_cvt_f64_f32_e32 v[108:109], v167
	v_fmac_f64_e32 v[94:95], v[106:107], v[108:109]
	s_waitcnt lgkmcnt(8)
	v_cvt_f64_f32_e32 v[106:107], v176
	s_waitcnt vmcnt(8)
	v_cvt_f64_f32_e32 v[108:109], v184
	v_fmac_f64_e32 v[92:93], v[106:107], v[108:109]
	v_cvt_f64_f32_e32 v[106:107], v177
	v_cvt_f64_f32_e32 v[108:109], v185
	v_fmac_f64_e32 v[94:95], v[106:107], v[108:109]
	v_cvt_f64_f32_e32 v[106:107], v178
	v_cvt_f64_f32_e32 v[108:109], v186
	v_fmac_f64_e32 v[92:93], v[106:107], v[108:109]
	v_cvt_f64_f32_e32 v[106:107], v179
	v_cvt_f64_f32_e32 v[108:109], v187
	v_fmac_f64_e32 v[94:95], v[106:107], v[108:109]
	v_cvt_f64_f32_e32 v[106:107], v172
	v_cvt_f64_f32_e32 v[108:109], v180
	v_fmac_f64_e32 v[92:93], v[106:107], v[108:109]
	v_cvt_f64_f32_e32 v[106:107], v173
	v_cvt_f64_f32_e32 v[108:109], v181
	v_fmac_f64_e32 v[94:95], v[106:107], v[108:109]
	v_cvt_f64_f32_e32 v[106:107], v174
	v_cvt_f64_f32_e32 v[108:109], v182
	v_fmac_f64_e32 v[92:93], v[106:107], v[108:109]
	v_cvt_f64_f32_e32 v[106:107], v175
	v_cvt_f64_f32_e32 v[108:109], v183
	v_fmac_f64_e32 v[94:95], v[106:107], v[108:109]
	s_waitcnt lgkmcnt(6)
	v_cvt_f64_f32_e32 v[106:107], v192
	s_waitcnt vmcnt(6)
	v_cvt_f64_f32_e32 v[108:109], v200
	v_fmac_f64_e32 v[92:93], v[106:107], v[108:109]
	v_cvt_f64_f32_e32 v[106:107], v193
	v_cvt_f64_f32_e32 v[108:109], v201
	v_fmac_f64_e32 v[94:95], v[106:107], v[108:109]
	v_cvt_f64_f32_e32 v[106:107], v194
	v_cvt_f64_f32_e32 v[108:109], v202
	v_fmac_f64_e32 v[92:93], v[106:107], v[108:109]
	v_cvt_f64_f32_e32 v[106:107], v195
	v_cvt_f64_f32_e32 v[108:109], v203
	v_fmac_f64_e32 v[94:95], v[106:107], v[108:109]
	v_cvt_f64_f32_e32 v[106:107], v188
	v_cvt_f64_f32_e32 v[108:109], v196
	v_fmac_f64_e32 v[92:93], v[106:107], v[108:109]
	v_cvt_f64_f32_e32 v[106:107], v189
	v_cvt_f64_f32_e32 v[108:109], v197
	v_fmac_f64_e32 v[94:95], v[106:107], v[108:109]
	v_cvt_f64_f32_e32 v[106:107], v190
	v_cvt_f64_f32_e32 v[108:109], v198
	v_fmac_f64_e32 v[92:93], v[106:107], v[108:109]
	v_cvt_f64_f32_e32 v[106:107], v191
	v_cvt_f64_f32_e32 v[108:109], v199
	v_fmac_f64_e32 v[94:95], v[106:107], v[108:109]
	s_waitcnt lgkmcnt(4)
	v_cvt_f64_f32_e32 v[106:107], v204
	s_waitcnt vmcnt(4)
	v_cvt_f64_f32_e32 v[108:109], v208
	v_fmac_f64_e32 v[92:93], v[106:107], v[108:109]
	v_cvt_f64_f32_e32 v[106:107], v205
	v_cvt_f64_f32_e32 v[108:109], v209
	v_fmac_f64_e32 v[94:95], v[106:107], v[108:109]
	v_cvt_f64_f32_e32 v[106:107], v206
	v_cvt_f64_f32_e32 v[108:109], v210
	v_fmac_f64_e32 v[92:93], v[106:107], v[108:109]
	v_cvt_f64_f32_e32 v[106:107], v207
	v_cvt_f64_f32_e32 v[108:109], v211
	v_fmac_f64_e32 v[94:95], v[106:107], v[108:109]
	v_cvt_f64_f32_e32 v[106:107], v74
	v_cvt_f64_f32_e32 v[108:109], v82
	v_cvt_f64_f32_e32 v[74:75], v75
	v_cvt_f64_f32_e32 v[82:83], v83
	v_fmac_f64_e32 v[92:93], v[106:107], v[108:109]
	v_fmac_f64_e32 v[94:95], v[74:75], v[82:83]
	v_cvt_f64_f32_e32 v[74:75], v76
	v_cvt_f64_f32_e32 v[82:83], v84
	v_fmac_f64_e32 v[92:93], v[74:75], v[82:83]
	v_cvt_f64_f32_e32 v[74:75], v77
	v_cvt_f64_f32_e32 v[76:77], v85
	v_fmac_f64_e32 v[94:95], v[74:75], v[76:77]
	s_waitcnt lgkmcnt(2)
	v_cvt_f64_f32_e32 v[74:75], v66
	s_waitcnt vmcnt(2)
	v_cvt_f64_f32_e32 v[76:77], v78
	v_fmac_f64_e32 v[92:93], v[74:75], v[76:77]
	v_cvt_f64_f32_e32 v[66:67], v67
	v_cvt_f64_f32_e32 v[74:75], v79
	v_fmac_f64_e32 v[94:95], v[66:67], v[74:75]
	v_cvt_f64_f32_e32 v[66:67], v68
	v_cvt_f64_f32_e32 v[74:75], v80
	v_fmac_f64_e32 v[92:93], v[66:67], v[74:75]
	v_cvt_f64_f32_e32 v[66:67], v69
	v_cvt_f64_f32_e32 v[68:69], v81
	v_fmac_f64_e32 v[94:95], v[66:67], v[68:69]
	v_cvt_f64_f32_e32 v[66:67], v54
	v_cvt_f64_f32_e32 v[68:69], v58
	v_cvt_f64_f32_e32 v[54:55], v55
	v_cvt_f64_f32_e32 v[58:59], v59
	v_fmac_f64_e32 v[92:93], v[66:67], v[68:69]
	v_fmac_f64_e32 v[94:95], v[54:55], v[58:59]
	v_cvt_f64_f32_e32 v[54:55], v56
	v_cvt_f64_f32_e32 v[58:59], v60
	v_fmac_f64_e32 v[92:93], v[54:55], v[58:59]
	v_cvt_f64_f32_e32 v[54:55], v57
	v_cvt_f64_f32_e32 v[56:57], v61
	v_fmac_f64_e32 v[94:95], v[54:55], v[56:57]
	s_waitcnt lgkmcnt(0)
	v_cvt_f64_f32_e32 v[54:55], v62
	s_waitcnt vmcnt(0)
	v_cvt_f64_f32_e32 v[56:57], v120
	v_fmac_f64_e32 v[92:93], v[54:55], v[56:57]
	v_cvt_f64_f32_e32 v[54:55], v63
	v_cvt_f64_f32_e32 v[56:57], v121
	v_fmac_f64_e32 v[94:95], v[54:55], v[56:57]
	v_cvt_f64_f32_e32 v[54:55], v64
	v_cvt_f64_f32_e32 v[56:57], v122
	v_fmac_f64_e32 v[92:93], v[54:55], v[56:57]
	v_cvt_f64_f32_e32 v[54:55], v65
	v_cvt_f64_f32_e32 v[56:57], v123
	v_fmac_f64_e32 v[94:95], v[54:55], v[56:57]
	v_cvt_f64_f32_e32 v[54:55], v50
	v_cvt_f64_f32_e32 v[56:57], v70
	v_fmac_f64_e32 v[92:93], v[54:55], v[56:57]
	v_cvt_f64_f32_e32 v[50:51], v51
	v_cvt_f64_f32_e32 v[54:55], v71
	v_fmac_f64_e32 v[94:95], v[50:51], v[54:55]
	v_cvt_f64_f32_e32 v[50:51], v52
	v_cvt_f64_f32_e32 v[54:55], v72
	v_fmac_f64_e32 v[92:93], v[50:51], v[54:55]
	v_cvt_f64_f32_e32 v[50:51], v53
	v_cvt_f64_f32_e32 v[52:53], v73
	v_fmac_f64_e32 v[94:95], v[50:51], v[52:53]
	v_add_f64 v[50:51], v[92:93], v[94:95]
	s_nop 1
	v_mov_b32_dpp v52, v50 quad_perm:[1,0,3,2] row_mask:0xf bank_mask:0xf
	v_mov_b32_dpp v53, v51 quad_perm:[1,0,3,2] row_mask:0xf bank_mask:0xf
	s_waitcnt lgkmcnt(0)
	v_add_f64 v[50:51], v[50:51], v[52:53]
	s_nop 1
	v_mov_b32_dpp v52, v50 quad_perm:[2,3,0,1] row_mask:0xf bank_mask:0xf
	v_mov_b32_dpp v53, v51 quad_perm:[2,3,0,1] row_mask:0xf bank_mask:0xf
	s_waitcnt lgkmcnt(0)
	v_add_f64 v[50:51], v[50:51], v[52:53]
	s_nop 1
	v_mov_b32_dpp v52, v50 row_half_mirror row_mask:0xf bank_mask:0xf
	v_mov_b32_dpp v53, v51 row_half_mirror row_mask:0xf bank_mask:0xf
	s_waitcnt lgkmcnt(0)
	v_add_f64 v[50:51], v[50:51], v[52:53]
	s_nop 1
	v_mov_b32_dpp v52, v50 row_mirror row_mask:0xf bank_mask:0xf
	v_mov_b32_dpp v53, v51 row_mirror row_mask:0xf bank_mask:0xf
	s_and_saveexec_b64 s[0:1], vcc
	s_cbranch_execz .LBB2_168
	v_lshrrev_b32_e32 v0, 8, v105
	v_lshl_add_u32 v0, v0, 3, 0
	v_lshl_add_u32 v54, v104, 3, 0
	v_add_u32_e32 v0, 0x13450, v0
	v_add_u32_e32 v56, 0x12ed0, v54
	ds_read_b64 v[54:55], v0
	ds_read_b64 v[56:57], v56
	s_waitcnt lgkmcnt(2)
	v_add_f64 v[50:51], v[50:51], v[52:53]
	s_waitcnt lgkmcnt(1)
	v_mul_f64 v[50:51], v[50:51], v[54:55]
	s_waitcnt lgkmcnt(0)
	v_mul_f64 v[50:51], v[50:51], v[56:57]
	ds_write_b64 v101, v[50:51]
	s_branch .LBB2_168
